# grid barrier: the follower that sees 8 workgroups of its XCD still to arrive pre-flushes the XCD L2 (buffer_wbl2 sc1) while it waits, shortening the XCD-last workgroup's release write-back
# baseline (speedup 1.0000x reference)
.LBB0_207:
	s_or_b64 exec, exec, s[10:11]
	v_cvt_f32_u32_e32 v4, v2
	s_waitcnt vmcnt(0)
	v_readfirstlane_b32 s8, v3
	v_sub_u32_e32 v3, 0, v2
	v_rcp_iflag_f32_e32 v4, v4
	v_add_u32_e32 v5, s8, v1
	v_mul_f32_e32 v4, 0x4f7ffffe, v4
	v_cvt_u32_f32_e32 v4, v4
	v_mul_lo_u32 v1, v3, v4
	v_mul_hi_u32 v1, v4, v1
	v_add_u32_e32 v1, v4, v1
	v_mul_hi_u32 v1, v5, v1
	v_mul_lo_u32 v3, v1, v2
	v_sub_u32_e32 v3, v5, v3
	v_add_u32_e32 v4, 1, v1
	v_cmp_ge_u32_e32 vcc, v3, v2
	s_nop 1
	v_cndmask_b32_e32 v1, v1, v4, vcc
	v_sub_u32_e32 v4, v3, v2
	v_cndmask_b32_e32 v3, v3, v4, vcc
	v_add_u32_e32 v4, 1, v1
	v_cmp_ge_u32_e32 vcc, v3, v2
	v_add_u32_e32 v3, 1, v5
	s_nop 0
	v_cndmask_b32_e32 v1, v1, v4, vcc
	v_mul_lo_u32 v4, v2, v1
	v_add_u32_e32 v2, v4, v2
	v_cmp_ne_u32_e32 vcc, v3, v2
	s_and_saveexec_b64 s[8:9], vcc
	s_xor_b64 s[8:9], exec, s[8:9]
	s_cbranch_execz .LBB0_221
	buffer_inv sc1
	v_sub_u32_e32 v4, v2, v3
	v_cmp_eq_u32_e32 vcc, 8, v4
	s_cbranch_vccz .Lbar_nf_0
	buffer_wbl2 sc1
.Lbar_nf_0:
	s_waitcnt lgkmcnt(0)
	v_mov_b32_e32 v0, 0x2000
	global_load_dword v0, v0, s[6:7] offset:1024 sc1
	s_add_u32 s14, s6, 0x2400
	s_addc_u32 s15, s7, 0
	s_waitcnt vmcnt(0)
	v_cmp_eq_u32_e32 vcc, v0, v1
	s_and_saveexec_b64 s[10:11], vcc
	s_cbranch_execz .LBB0_220
	s_add_u32 s12, s84, 0x4200
	s_addc_u32 s13, s85, 0
	s_mov_b32 s26, 1
	s_mov_b64 s[16:17], 0
	v_mov_b32_e32 v0, 0
	s_branch .LBB0_211

.LBB0_295:
	s_or_b64 exec, exec, s[6:7]
	v_cvt_f32_u32_e32 v5, v3
	s_waitcnt vmcnt(0)
	v_readfirstlane_b32 s6, v4
	v_sub_u32_e32 v4, 0, v3
	v_rcp_iflag_f32_e32 v5, v5
	v_add_u32_e32 v6, s6, v0
	v_mul_f32_e32 v5, 0x4f7ffffe, v5
	v_cvt_u32_f32_e32 v5, v5
	v_mul_lo_u32 v0, v4, v5
	v_mul_hi_u32 v0, v5, v0
	v_add_u32_e32 v0, v5, v0
	v_mul_hi_u32 v0, v6, v0
	v_mul_lo_u32 v4, v0, v3
	v_sub_u32_e32 v4, v6, v4
	v_add_u32_e32 v5, 1, v0
	v_cmp_ge_u32_e32 vcc, v4, v3
	s_nop 1
	v_cndmask_b32_e32 v0, v0, v5, vcc
	v_sub_u32_e32 v5, v4, v3
	v_cndmask_b32_e32 v4, v4, v5, vcc
	v_add_u32_e32 v5, 1, v0
	v_cmp_ge_u32_e32 vcc, v4, v3
	v_add_u32_e32 v4, 1, v6
	s_nop 0
	v_cndmask_b32_e32 v0, v0, v5, vcc
	v_mul_lo_u32 v5, v3, v0
	v_add_u32_e32 v3, v5, v3
	v_cmp_ne_u32_e32 vcc, v4, v3
	s_and_saveexec_b64 s[6:7], vcc
	s_xor_b64 s[6:7], exec, s[6:7]
	s_cbranch_execz .LBB0_309
	buffer_inv sc1
	v_sub_u32_e32 v5, v3, v4
	v_cmp_eq_u32_e32 vcc, 8, v5
	s_cbranch_vccz .Lbar_nf_1
	buffer_wbl2 sc1
.Lbar_nf_1:
	v_readlane_b32 s8, v254, 5
	v_readlane_b32 s9, v254, 6
	s_waitcnt lgkmcnt(0)
	s_nop 3
	global_load_dword v2, v1, s[8:9] sc1
	s_waitcnt vmcnt(0)
	v_cmp_eq_u32_e32 vcc, v2, v0
	s_and_saveexec_b64 s[8:9], vcc
	s_cbranch_execz .LBB0_308
	s_mov_b32 s24, 1
	s_mov_b64 s[10:11], 0
	s_branch .LBB0_299

.Lbar_nf_10:
	v_readlane_b32 s8, v254, 5
	v_readlane_b32 s9, v254, 6
	s_waitcnt lgkmcnt(0)
	s_nop 3
	global_load_dword v2, v1, s[8:9] sc1
	s_waitcnt vmcnt(0)
	v_cmp_eq_u32_e32 vcc, v2, v0
	s_and_saveexec_b64 s[8:9], vcc
	s_cbranch_execz .LBB0_1586
	s_mov_b32 s20, 1
	s_mov_b64 s[10:11], 0
	s_branch .LBB0_1577
